# nt also on layer-1 router row loads and the final output stores (never re-read)
# baseline (speedup 1.0000x reference)
.LBB0_1821:
	v_lshl_add_u64 v[140:141], s[8:9], 0, v[138:139]
	v_add_co_u32_e32 v66, vcc, 0x29100000, v140
	s_nop 1
	v_addc_co_u32_e32 v67, vcc, 0, v141, vcc
	global_load_dwordx2 v[142:143], v[66:67], off offset:1536 nt
	global_load_dwordx2 v[144:145], v[66:67], off offset:2048 nt
	global_load_dwordx2 v[160:161], v[66:67], off offset:3072 nt
	global_load_dwordx2 v[162:163], v[66:67], off offset:3584 nt
	global_load_dwordx2 v[164:165], v[66:67], off offset:512 nt
	global_load_dwordx2 v[166:167], v[66:67], off offset:1024 nt
	global_load_dwordx2 v[168:169], v[66:67], off nt
	global_load_dwordx2 v[170:171], v[66:67], off offset:2560 nt
	global_load_dwordx4 v[70:73], v[90:91], off nt
	global_load_dwordx4 v[74:77], v[92:93], off nt
	s_waitcnt lgkmcnt(0)
	global_load_dwordx4 v[66:69], v[94:95], off nt
	global_load_dwordx4 v[86:89], v[96:97], off nt
	global_load_dwordx4 v[82:85], v[98:99], off nt
	global_load_dwordx4 v[78:81], v[100:101], off nt
	global_load_dwordx4 v[156:159], v[102:103], off nt
	s_waitcnt vmcnt(14)
	v_lshlrev_b32_e32 v220, 16, v142
	v_and_b32_e32 v221, 0xffff0000, v142
	s_waitcnt vmcnt(13)
	v_lshlrev_b32_e32 v222, 16, v144
	v_and_b32_e32 v155, 0xffff0000, v144
	s_waitcnt vmcnt(10)
	v_and_b32_e32 v229, 0xffff0000, v164
	v_and_b32_e32 v233, 0xffff0000, v165
	s_waitcnt vmcnt(8)
	v_and_b32_e32 v228, 0xffff0000, v168
	v_and_b32_e32 v232, 0xffff0000, v169
	v_lshlrev_b32_e32 v224, 16, v145
	v_and_b32_e32 v225, 0xffff0000, v145
	v_lshlrev_b32_e32 v146, 16, v160
	v_and_b32_e32 v147, 0xffff0000, v160
	v_lshlrev_b32_e32 v142, 16, v162
	v_and_b32_e32 v250, 0xffff0000, v162
	v_lshlrev_b32_e32 v144, 16, v163
	v_and_b32_e32 v145, 0xffff0000, v163
	v_lshlrev_b32_e32 v227, 16, v164
	v_lshlrev_b32_e32 v226, 16, v168
	v_lshlrev_b32_e32 v231, 16, v165
	v_lshlrev_b32_e32 v230, 16, v169
	v_and_b32_e32 v237, 0xffff0000, v167
	v_and_b32_e32 v236, 0xffff0000, v166
	v_lshlrev_b32_e32 v244, 16, v161
	v_and_b32_e32 v245, 0xffff0000, v161
	v_pk_mul_f32 v[160:161], v[228:229], v[228:229]
	v_pk_mul_f32 v[162:163], v[232:233], v[232:233]
	v_lshlrev_b32_e32 v235, 16, v167
	v_lshlrev_b32_e32 v234, 16, v166
	v_lshlrev_b32_e32 v238, 16, v143
	v_pk_mul_f32 v[164:165], v[236:237], v[236:237]
	v_pk_fma_f32 v[160:161], v[226:227], v[226:227], v[160:161]
	v_pk_fma_f32 v[162:163], v[230:231], v[230:231], v[162:163]
	v_and_b32_e32 v239, 0xffff0000, v143
	v_mul_f32_e32 v223, v220, v220
	v_mul_f32_e32 v167, v221, v221
	v_mul_f32_e32 v168, v238, v238
	v_mov_b32_e32 v166, v222
	v_pk_fma_f32 v[164:165], v[234:235], v[234:235], v[164:165]
	v_pk_add_f32 v[160:161], v[160:161], v[162:163]
	v_pk_fma_f32 v[168:169], v[238:239], v[238:239], v[168:169] op_sel_hi:[1,1,0]
	v_pk_add_f32 v[166:167], v[222:223], v[166:167]
	v_pk_add_f32 v[162:163], v[164:165], v[164:165] op_sel_hi:[0,1]
	v_pk_add_f32 v[160:161], v[160:161], v[160:161] op_sel_hi:[0,1]
	s_waitcnt vmcnt(7)
	v_lshlrev_b32_e32 v241, 16, v171
	v_lshlrev_b32_e32 v240, 16, v170
	v_and_b32_e32 v243, 0xffff0000, v171
	v_and_b32_e32 v242, 0xffff0000, v170
	v_mul_f32_e32 v170, v222, v222
	v_mul_f32_e32 v168, v155, v155
	v_mov_b32_e32 v171, v167
	v_mul_f32_e32 v162, v224, v224
	v_mul_f32_e32 v160, v225, v225
	v_pk_mul_f32 v[172:173], v[242:243], v[242:243]
	v_pk_add_f32 v[166:167], v[170:171], v[168:169]
	v_pk_add_f32 v[160:161], v[162:163], v[160:161]
	v_mul_f32_e32 v143, v146, v146
	v_mul_f32_e32 v175, v147, v147
	v_mul_f32_e32 v176, v244, v244
	v_mov_b32_e32 v174, v142
	v_pk_fma_f32 v[172:173], v[240:241], v[240:241], v[172:173]
	v_pk_add_f32 v[160:161], v[166:167], v[160:161]
	v_pk_fma_f32 v[176:177], v[244:245], v[244:245], v[176:177] op_sel_hi:[1,1,0]
	v_pk_add_f32 v[174:175], v[142:143], v[174:175]
	v_pk_add_f32 v[164:165], v[172:173], v[172:173] op_sel_hi:[0,1]
	v_pk_add_f32 v[160:161], v[160:161], v[160:161] op_sel_hi:[0,1]
	v_mul_f32_e32 v178, v142, v142
	v_mul_f32_e32 v176, v250, v250
	v_mov_b32_e32 v179, v175
	v_mul_f32_e32 v164, v144, v144
	v_mul_f32_e32 v160, v145, v145
	v_pk_add_f32 v[168:169], v[178:179], v[176:177]
	v_pk_add_f32 v[160:161], v[164:165], v[160:161]
	s_waitcnt vmcnt(5)
	v_pk_add_f32 v[246:247], v[74:75], 1.0 op_sel_hi:[1,0]
	v_pk_add_f32 v[160:161], v[168:169], v[160:161]
	v_mov_b32_e32 v74, v230
	v_add_f32_e32 v143, v160, v161
	ds_bpermute_b32 v168, v148, v143
	global_load_dwordx4 v[160:163], v[104:105], off nt
	global_load_dwordx4 v[164:167], v[106:107], off nt
	v_mov_b32_e32 v248, v226
	v_mov_b32_e32 v249, v228
	v_pk_add_f32 v[76:77], v[76:77], 1.0 op_sel_hi:[1,0]
	s_waitcnt lgkmcnt(0)
	v_add_f32_e32 v143, v143, v168
	ds_bpermute_b32 v180, v149, v143
	global_load_dwordx4 v[168:171], v[108:109], off nt
	global_load_dwordx4 v[172:175], v[110:111], off nt
	global_load_dwordx4 v[176:179], v[112:113], off nt
	v_mov_b32_e32 v228, v227
	s_waitcnt vmcnt(7)
	v_pk_add_f32 v[82:83], v[82:83], 1.0 op_sel_hi:[1,0]
	v_pk_add_f32 v[84:85], v[84:85], 1.0 op_sel_hi:[1,0]
	s_waitcnt lgkmcnt(0)
	v_add_f32_e32 v143, v143, v180
	ds_bpermute_b32 v184, v150, v143
	global_load_dwordx4 v[180:183], v[114:115], off nt
	s_waitcnt lgkmcnt(0)
	v_add_f32_e32 v143, v143, v184
	ds_bpermute_b32 v196, v151, v143
	global_load_dwordx4 v[184:187], v[116:117], off nt
	global_load_dwordx4 v[188:191], v[118:119], off nt
	global_load_dwordx4 v[192:195], v[120:121], off nt
	s_waitcnt lgkmcnt(0)
	v_add_f32_e32 v143, v143, v196
	ds_bpermute_b32 v216, v152, v143
	global_load_dwordx4 v[196:199], v[122:123], off nt
	global_load_dwordx4 v[200:203], v[124:125], off nt
	global_load_dwordx4 v[204:207], v[126:127], off nt
	global_load_dwordx4 v[208:211], v[128:129], off nt
	global_load_dwordx4 v[212:215], v[130:131], off nt
	s_waitcnt lgkmcnt(0)
	v_add_f32_e32 v143, v143, v216
	ds_bpermute_b32 v223, v153, v143
	global_load_dwordx4 v[216:219], v[132:133], off nt
	s_waitcnt lgkmcnt(0)
	v_add_f32_e32 v75, v143, v223
	v_fmamk_f32 v75, v75, 0x3a000000, v154
	v_rsq_f32_e32 v230, v75
	v_mov_b32_e32 v75, v232
	v_mov_b32_e32 v232, v231
	v_mov_b32_e32 v223, v155
	v_pk_mul_f32 v[74:75], v[74:75], v[230:231] op_sel_hi:[1,0]
	v_pk_mul_f32 v[248:249], v[248:249], v[230:231] op_sel_hi:[1,0]
	v_pk_mul_f32 v[74:75], v[72:73], v[74:75]
	v_pk_mul_f32 v[248:249], v[70:71], v[248:249]
	global_load_dwordx4 v[70:73], v[134:135], off nt
	v_pk_fma_f32 v[68:69], v[76:77], v[74:75], v[68:69]
	global_load_dwordx4 v[74:77], v[136:137], off nt
	v_pk_mul_f32 v[226:227], v[228:229], v[230:231] op_sel_hi:[1,0]
	v_pk_mul_f32 v[232:233], v[232:233], v[230:231] op_sel_hi:[1,0]
	v_pk_mul_f32 v[86:87], v[86:87], v[226:227]
	v_pk_mul_f32 v[88:89], v[88:89], v[232:233]
	s_waitcnt vmcnt(18)
	v_pk_fma_f32 v[78:79], v[82:83], v[86:87], v[78:79]
	v_mov_b32_e32 v82, v235
	v_mov_b32_e32 v83, v237
	v_pk_mul_f32 v[82:83], v[230:231], v[82:83] op_sel_hi:[0,1]
	v_mov_b32_e32 v235, v236
	s_waitcnt vmcnt(17)
	v_pk_mul_f32 v[82:83], v[158:159], v[82:83]
	v_pk_fma_f32 v[80:81], v[84:85], v[88:89], v[80:81]
	v_pk_mul_f32 v[84:85], v[230:231], v[234:235] op_sel_hi:[0,1]
	v_pk_mul_f32 v[84:85], v[156:157], v[84:85]
	v_pk_mul_f32 v[144:145], v[144:145], v[230:231] op_sel_hi:[1,0]
	v_mov_b32_e32 v143, v250
	v_pk_mul_f32 v[146:147], v[146:147], v[230:231] op_sel_hi:[1,0]
	v_pk_mul_f32 v[142:143], v[142:143], v[230:231] op_sel_hi:[1,0]
	v_mov_b32_e32 v155, v1
	v_pk_fma_f32 v[66:67], v[246:247], v[248:249], v[66:67]
	s_waitcnt vmcnt(16)
	v_pk_add_f32 v[86:87], v[162:163], 1.0 op_sel_hi:[1,0]
	s_waitcnt vmcnt(15)
	v_pk_fma_f32 v[82:83], v[86:87], v[82:83], v[166:167]
	v_pk_mul_f32 v[86:87], v[238:239], v[230:231] op_sel_hi:[1,0]
	v_pk_add_f32 v[88:89], v[160:161], 1.0 op_sel_hi:[1,0]
	s_waitcnt vmcnt(14)
	v_pk_mul_f32 v[86:87], v[170:171], v[86:87]
	s_waitcnt vmcnt(13)
	v_pk_add_f32 v[156:157], v[174:175], 1.0 op_sel_hi:[1,0]
	v_pk_fma_f32 v[84:85], v[88:89], v[84:85], v[164:165]
	v_pk_mul_f32 v[88:89], v[220:221], v[230:231] op_sel_hi:[1,0]
	s_waitcnt vmcnt(12)
	v_pk_fma_f32 v[86:87], v[156:157], v[86:87], v[178:179]
	v_pk_mul_f32 v[156:157], v[224:225], v[230:231] op_sel_hi:[1,0]
	v_pk_mul_f32 v[88:89], v[168:169], v[88:89]
	v_pk_add_f32 v[158:159], v[172:173], 1.0 op_sel_hi:[1,0]
	s_waitcnt vmcnt(11)
	v_pk_mul_f32 v[156:157], v[156:157], v[182:183]
	v_pk_fma_f32 v[88:89], v[158:159], v[88:89], v[176:177]
	v_pk_mul_f32 v[158:159], v[222:223], v[230:231] op_sel_hi:[1,0]
	s_waitcnt vmcnt(10)
	v_pk_add_f32 v[160:161], v[186:187], 1.0 op_sel_hi:[1,0]
	s_waitcnt vmcnt(9)
	v_pk_fma_f32 v[156:157], v[156:157], v[160:161], v[190:191]
	v_mov_b32_e32 v160, v241
	v_mov_b32_e32 v161, v243
	v_pk_mul_f32 v[158:159], v[158:159], v[180:181]
	v_pk_add_f32 v[162:163], v[184:185], 1.0 op_sel_hi:[1,0]
	v_pk_mul_f32 v[160:161], v[230:231], v[160:161] op_sel_hi:[0,1]
	v_mov_b32_e32 v241, v242
	v_pk_fma_f32 v[158:159], v[158:159], v[162:163], v[188:189]
	v_pk_mul_f32 v[162:163], v[230:231], v[240:241] op_sel_hi:[0,1]
	s_waitcnt vmcnt(8)
	v_pk_mul_f32 v[160:161], v[160:161], v[194:195]
	s_waitcnt vmcnt(7)
	v_pk_add_f32 v[164:165], v[198:199], 1.0 op_sel_hi:[1,0]
	v_pk_mul_f32 v[162:163], v[162:163], v[192:193]
	v_pk_add_f32 v[166:167], v[196:197], 1.0 op_sel_hi:[1,0]
	s_waitcnt vmcnt(2)
	v_pk_mul_f32 v[144:145], v[144:145], v[218:219]
	v_pk_fma_f32 v[160:161], v[160:161], v[164:165], v[202:203]
	v_pk_mul_f32 v[164:165], v[244:245], v[230:231] op_sel_hi:[1,0]
	v_pk_fma_f32 v[162:163], v[162:163], v[166:167], v[200:201]
	v_pk_mul_f32 v[146:147], v[146:147], v[204:205]
	v_pk_mul_f32 v[164:165], v[164:165], v[206:207]
	v_pk_add_f32 v[166:167], v[210:211], 1.0 op_sel_hi:[1,0]
	v_pk_add_f32 v[168:169], v[208:209], 1.0 op_sel_hi:[1,0]
	v_pk_mul_f32 v[142:143], v[142:143], v[216:217]
	v_pk_fma_f32 v[164:165], v[164:165], v[166:167], v[214:215]
	v_pk_fma_f32 v[146:147], v[146:147], v[168:169], v[212:213]
	v_cvt_pk_bf16_f32 v166, v158, v159
	v_cvt_pk_bf16_f32 v167, v156, v157
	v_cvt_pk_bf16_f32 v168, v162, v163
	s_waitcnt vmcnt(1)
	v_pk_add_f32 v[72:73], v[72:73], 1.0 op_sel_hi:[1,0]
	v_pk_add_f32 v[70:71], v[70:71], 1.0 op_sel_hi:[1,0]
	s_waitcnt vmcnt(0)
	v_pk_fma_f32 v[72:73], v[144:145], v[72:73], v[76:77]
	v_add_co_u32_e32 v76, vcc, s11, v140
	v_pk_fma_f32 v[70:71], v[142:143], v[70:71], v[74:75]
	s_nop 0
	v_addc_co_u32_e32 v77, vcc, 0, v141, vcc
	v_cvt_pk_bf16_f32 v74, v66, v67
	v_cvt_pk_bf16_f32 v75, v68, v69
	global_store_dwordx2 v[76:77], v[74:75], off
	v_cvt_pk_bf16_f32 v140, v78, v79
	v_cvt_pk_bf16_f32 v141, v80, v81
	global_store_dwordx2 v[76:77], v[140:141], off offset:512
	v_cvt_pk_bf16_f32 v142, v84, v85
	v_cvt_pk_bf16_f32 v143, v82, v83
	global_store_dwordx2 v[76:77], v[142:143], off offset:1024
	v_cvt_pk_bf16_f32 v144, v88, v89
	v_cvt_pk_bf16_f32 v145, v86, v87
	global_store_dwordx2 v[76:77], v[144:145], off offset:1536
	global_store_dwordx2 v[76:77], v[166:167], off offset:2048
	v_cvt_pk_bf16_f32 v169, v160, v161
	global_store_dwordx2 v[76:77], v[168:169], off offset:2560
	v_cvt_pk_bf16_f32 v170, v146, v147
	v_cvt_pk_bf16_f32 v171, v164, v165
	global_store_dwordx2 v[76:77], v[170:171], off offset:3072
	v_cvt_pk_bf16_f32 v172, v70, v71
	v_cvt_pk_bf16_f32 v173, v72, v73
	global_store_dwordx2 v[76:77], v[172:173], off offset:3584
	s_barrier
	s_nop 0
	v_lshlrev_b32_e32 v76, 3, v155
	v_and_b32_e32 v174, 8, v76
	v_lshlrev_b32_e32 v76, 16, v74
	v_sub_f32_e32 v66, v66, v76
	v_and_b32_e32 v76, 0xffff0000, v74
	v_sub_f32_e32 v67, v67, v76
	v_cvt_pk_bf16_f32 v66, v66, v67
	v_lshlrev_b32_e32 v67, 16, v75
	v_sub_f32_e32 v67, v68, v67
	v_and_b32_e32 v68, 0xffff0000, v75
	v_sub_f32_e32 v68, v69, v68
	v_lshrrev_b32_e32 v176, 1, v155
	v_or_b32_e32 v175, s4, v174
	v_cvt_pk_bf16_f32 v67, v67, v68
	v_xor_b32_e32 v68, s3, v176
	v_lshl_add_u32 v68, v68, 4, v175
	v_add_u32_e32 v69, 0, v68
	v_add_u32_e32 v68, s21, v68
	ds_write_b64 v69, v[74:75]
	ds_write_b64 v68, v[66:67]
	v_lshlrev_b32_e32 v68, 16, v140
	v_and_b32_e32 v69, 0xffff0000, v140
	v_sub_f32_e32 v68, v78, v68
	v_sub_f32_e32 v69, v79, v69
	v_cvt_pk_bf16_f32 v68, v68, v69
	v_lshlrev_b32_e32 v69, 16, v141
	v_and_b32_e32 v76, 0xffff0000, v141
	v_sub_f32_e32 v69, v80, v69
	v_sub_f32_e32 v76, v81, v76
	v_cvt_pk_bf16_f32 v69, v69, v76
	v_add_u32_e32 v76, 64, v155
	v_lshrrev_b32_e32 v177, 1, v76
	v_xor_b32_e32 v76, s3, v177
	v_lshl_add_u32 v76, v76, 4, v175
	v_add_u32_e32 v77, 0, v76
	v_add_u32_e32 v76, s21, v76
	ds_write_b64 v77, v[140:141]
	ds_write_b64 v76, v[68:69]
	v_lshlrev_b32_e32 v76, 16, v142
	v_and_b32_e32 v77, 0xffff0000, v142
	v_sub_f32_e32 v76, v84, v76
	v_sub_f32_e32 v77, v85, v77
	v_cvt_pk_bf16_f32 v76, v76, v77
	v_lshlrev_b32_e32 v77, 16, v143
	v_and_b32_e32 v78, 0xffff0000, v143
	v_sub_f32_e32 v77, v82, v77
	v_sub_f32_e32 v78, v83, v78
	v_cvt_pk_bf16_f32 v77, v77, v78
	v_add_u32_e32 v78, 0x80, v155
	v_lshrrev_b32_e32 v178, 1, v78
	v_xor_b32_e32 v78, s3, v178
	v_lshl_add_u32 v78, v78, 4, v175
	v_add_u32_e32 v79, 0, v78
	v_add_u32_e32 v78, s21, v78
	ds_write_b64 v79, v[142:143]
	ds_write_b64 v78, v[76:77]
	v_lshlrev_b32_e32 v78, 16, v144
	v_and_b32_e32 v79, 0xffff0000, v144
	v_sub_f32_e32 v78, v88, v78
	v_sub_f32_e32 v79, v89, v79
	v_cvt_pk_bf16_f32 v78, v78, v79
	v_lshlrev_b32_e32 v79, 16, v145
	v_and_b32_e32 v80, 0xffff0000, v145
	v_sub_f32_e32 v79, v86, v79
	v_sub_f32_e32 v80, v87, v80
	v_cvt_pk_bf16_f32 v79, v79, v80
	v_add_u32_e32 v80, 0xc0, v155
	v_lshrrev_b32_e32 v86, 1, v80
	v_xor_b32_e32 v80, s3, v86
	v_lshl_add_u32 v80, v80, 4, v175
	v_add_u32_e32 v81, 0, v80
	v_add_u32_e32 v80, s21, v80
	ds_write_b64 v81, v[144:145]
	ds_write_b64 v80, v[78:79]
	v_lshlrev_b32_e32 v80, 16, v166
	v_and_b32_e32 v81, 0xffff0000, v166
	v_sub_f32_e32 v80, v158, v80
	v_sub_f32_e32 v81, v159, v81
	v_cvt_pk_bf16_f32 v80, v80, v81
	v_lshlrev_b32_e32 v81, 16, v167
	v_and_b32_e32 v82, 0xffff0000, v167
	v_sub_f32_e32 v81, v156, v81
	v_sub_f32_e32 v82, v157, v82
	v_cvt_pk_bf16_f32 v81, v81, v82
	v_add_u32_e32 v82, 0x100, v155
	v_lshrrev_b32_e32 v87, 1, v82
	v_xor_b32_e32 v82, s3, v87
	v_lshl_add_u32 v82, v82, 4, v175
	v_add_u32_e32 v83, 0, v82
	v_add_u32_e32 v82, s21, v82
	ds_write_b64 v83, v[166:167]
	ds_write_b64 v82, v[80:81]
	v_lshlrev_b32_e32 v82, 16, v168
	v_and_b32_e32 v83, 0xffff0000, v168
	v_sub_f32_e32 v82, v162, v82
	v_sub_f32_e32 v83, v163, v83
	v_cvt_pk_bf16_f32 v82, v82, v83
	v_lshlrev_b32_e32 v83, 16, v169
	v_and_b32_e32 v84, 0xffff0000, v169
	v_sub_f32_e32 v83, v160, v83
	v_sub_f32_e32 v84, v161, v84
	v_cvt_pk_bf16_f32 v83, v83, v84
	v_add_u32_e32 v84, 0x140, v155
	v_lshrrev_b32_e32 v88, 1, v84
	v_xor_b32_e32 v84, s3, v88
	v_lshl_add_u32 v84, v84, 4, v175
	v_add_u32_e32 v85, 0, v84
	v_add_u32_e32 v84, s21, v84
	ds_write_b64 v85, v[168:169]
	ds_write_b64 v84, v[82:83]
	v_lshlrev_b32_e32 v84, 16, v170
	v_and_b32_e32 v85, 0xffff0000, v170
	v_sub_f32_e32 v84, v146, v84
	v_sub_f32_e32 v85, v147, v85
	v_cvt_pk_bf16_f32 v84, v84, v85
	v_lshlrev_b32_e32 v85, 16, v171
	v_and_b32_e32 v89, 0xffff0000, v171
	v_sub_f32_e32 v85, v164, v85
	v_sub_f32_e32 v89, v165, v89
	v_cvt_pk_bf16_f32 v85, v85, v89
	v_add_u32_e32 v89, 0x180, v155
	v_lshrrev_b32_e32 v89, 1, v89
	v_xor_b32_e32 v146, s3, v89
	v_lshl_add_u32 v146, v146, 4, v175
	v_add_u32_e32 v147, 0, v146
	v_add_u32_e32 v146, s21, v146
	ds_write_b64 v146, v[84:85]
	v_lshlrev_b32_e32 v146, 16, v172
	v_sub_f32_e32 v70, v70, v146
	v_and_b32_e32 v146, 0xffff0000, v172
	v_sub_f32_e32 v71, v71, v146
	v_cvt_pk_bf16_f32 v70, v70, v71
	v_lshlrev_b32_e32 v71, 16, v173
	v_sub_f32_e32 v71, v72, v71
	v_and_b32_e32 v72, 0xffff0000, v173
	v_sub_f32_e32 v72, v73, v72
	v_cvt_pk_bf16_f32 v71, v71, v72
	v_add_u32_e32 v72, 0x1c0, v155
	v_lshrrev_b32_e32 v72, 1, v72
	v_xor_b32_e32 v73, s3, v72
	v_lshl_add_u32 v73, v73, 4, v175
	v_add_u32_e32 v146, 0, v73
	v_add_u32_e32 v73, s21, v73
	ds_write_b64 v147, v[170:171]
	ds_write_b64 v146, v[172:173]
	ds_write_b64 v73, v[70:71]
	v_or_b32_e32 v73, s16, v174
	v_xor_b32_e32 v146, s5, v176
	v_lshl_add_u32 v146, v146, 4, v73
	v_add_u32_e32 v147, 0, v146
	ds_write_b64 v147, v[74:75]
	v_add_u32_e32 v74, s21, v146
	ds_write_b64 v74, v[66:67]
	v_xor_b32_e32 v66, s5, v177
	v_lshl_add_u32 v66, v66, 4, v73
	v_add_u32_e32 v67, 0, v66
	v_add_u32_e32 v66, s21, v66
	ds_write_b64 v66, v[68:69]
	v_xor_b32_e32 v66, s5, v178
	v_lshl_add_u32 v66, v66, 4, v73
	ds_write_b64 v67, v[140:141]
	v_add_u32_e32 v67, 0, v66
	v_add_u32_e32 v66, s21, v66
	ds_write_b64 v66, v[76:77]
	v_xor_b32_e32 v66, s5, v86
	v_lshl_add_u32 v66, v66, 4, v73
	ds_write_b64 v67, v[142:143]
	v_add_u32_e32 v67, 0, v66
	v_add_u32_e32 v66, s21, v66
	ds_write_b64 v66, v[78:79]
	v_xor_b32_e32 v66, s5, v87
	v_lshl_add_u32 v66, v66, 4, v73
	ds_write_b64 v67, v[144:145]
	v_add_u32_e32 v67, 0, v66
	v_add_u32_e32 v66, s21, v66
	ds_write_b64 v66, v[80:81]
	v_xor_b32_e32 v66, s5, v88
	v_lshl_add_u32 v66, v66, 4, v73
	ds_write_b64 v67, v[166:167]
	v_add_u32_e32 v67, 0, v66
	v_add_u32_e32 v66, s21, v66
	ds_write_b64 v66, v[82:83]
	v_xor_b32_e32 v66, s5, v89
	v_lshl_add_u32 v66, v66, 4, v73
	ds_write_b64 v67, v[168:169]
	v_add_u32_e32 v67, 0, v66
	v_add_u32_e32 v66, s21, v66
	ds_write_b64 v66, v[84:85]
	v_xor_b32_e32 v66, s5, v72
	v_lshl_add_u32 v66, v66, 4, v73
	ds_write_b64 v67, v[170:171]
	v_add_u32_e32 v67, 0, v66
	ds_write_b64 v67, v[172:173]
	v_add_u32_e32 v66, s21, v66
	v_lshrrev_b32_e32 v67, 4, v155
	ds_write_b64 v66, v[70:71]
	v_and_b32_e32 v66, 15, v155
	v_add_u32_e32 v67, s17, v67
	v_lshlrev_b32_e32 v80, 12, v66
	v_bitop3_b32 v68, v67, v155, 15 bitop3:0x78
	v_lshl_add_u32 v72, v68, 4, v80
	v_add_u32_e32 v68, 0, v72
	s_waitcnt lgkmcnt(0)
	s_barrier
	ds_read_b128 v[68:71], v68
	v_add_u32_e32 v72, s21, v72
	ds_read_b128 v[72:75], v72
	s_waitcnt lgkmcnt(1)
	v_mfma_f32_16x16x32_bf16 v[76:79], v[2:5], v[68:71], 0
	v_cmp_gt_u32_e32 vcc, 32, v155
	s_waitcnt lgkmcnt(0)
	v_mfma_f32_16x16x32_bf16 v[72:75], v[2:5], v[72:75], v[76:79]
	v_mfma_f32_16x16x32_bf16 v[68:71], v[6:9], v[68:71], v[72:75]
	s_nop 6
	v_add_u32_e32 v72, 4, v67
	v_bitop3_b32 v72, v72, v155, 15 bitop3:0x78
	v_lshl_add_u32 v76, v72, 4, v80
	v_add_u32_e32 v72, 0, v76
	ds_read_b128 v[72:75], v72
	v_add_u32_e32 v76, s21, v76
	ds_read_b128 v[76:79], v76
	s_waitcnt lgkmcnt(1)
	v_mfma_f32_16x16x32_bf16 v[68:71], v[10:13], v[72:75], v[68:71]
	s_waitcnt lgkmcnt(0)
	v_mfma_f32_16x16x32_bf16 v[68:71], v[10:13], v[76:79], v[68:71]
	v_mfma_f32_16x16x32_bf16 v[68:71], v[14:17], v[72:75], v[68:71]
	v_add_u32_e32 v72, 8, v67
	v_bitop3_b32 v72, v72, v155, 15 bitop3:0x78
	v_lshl_add_u32 v76, v72, 4, v80
	v_add_u32_e32 v72, 0, v76
	ds_read_b128 v[72:75], v72
	v_add_u32_e32 v76, s21, v76
	ds_read_b128 v[76:79], v76
	s_waitcnt lgkmcnt(1)
	v_mfma_f32_16x16x32_bf16 v[68:71], v[18:21], v[72:75], v[68:71]
	s_waitcnt lgkmcnt(0)
	v_mfma_f32_16x16x32_bf16 v[68:71], v[18:21], v[76:79], v[68:71]
	v_mfma_f32_16x16x32_bf16 v[68:71], v[22:25], v[72:75], v[68:71]
	v_add_u32_e32 v72, 12, v67
	v_bitop3_b32 v72, v72, v155, 15 bitop3:0x78
	v_lshl_add_u32 v76, v72, 4, v80
	v_add_u32_e32 v72, 0, v76
	ds_read_b128 v[72:75], v72
	v_add_u32_e32 v76, s21, v76
	ds_read_b128 v[76:79], v76
	s_waitcnt lgkmcnt(1)
	v_mfma_f32_16x16x32_bf16 v[68:71], v[26:29], v[72:75], v[68:71]
	s_waitcnt lgkmcnt(0)
	v_mfma_f32_16x16x32_bf16 v[68:71], v[26:29], v[76:79], v[68:71]
	v_mfma_f32_16x16x32_bf16 v[68:71], v[30:33], v[72:75], v[68:71]
	v_add_u32_e32 v72, 16, v67
	v_bitop3_b32 v72, v72, v155, 15 bitop3:0x78
	v_lshl_add_u32 v76, v72, 4, v80
	v_add_u32_e32 v72, 0, v76
	ds_read_b128 v[72:75], v72
	v_add_u32_e32 v76, s21, v76
	ds_read_b128 v[76:79], v76
	s_waitcnt lgkmcnt(1)
	v_mfma_f32_16x16x32_bf16 v[68:71], v[34:37], v[72:75], v[68:71]
	s_waitcnt lgkmcnt(0)
	v_mfma_f32_16x16x32_bf16 v[68:71], v[34:37], v[76:79], v[68:71]
	v_mfma_f32_16x16x32_bf16 v[68:71], v[38:41], v[72:75], v[68:71]
	v_add_u32_e32 v72, 20, v67
	v_bitop3_b32 v72, v72, v155, 15 bitop3:0x78
	v_lshl_add_u32 v76, v72, 4, v80
	v_add_u32_e32 v72, 0, v76
	ds_read_b128 v[72:75], v72
	v_add_u32_e32 v76, s21, v76
	ds_read_b128 v[76:79], v76
	s_waitcnt lgkmcnt(1)
	v_mfma_f32_16x16x32_bf16 v[68:71], v[42:45], v[72:75], v[68:71]
	s_waitcnt lgkmcnt(0)
	v_mfma_f32_16x16x32_bf16 v[68:71], v[42:45], v[76:79], v[68:71]
	v_mfma_f32_16x16x32_bf16 v[68:71], v[46:49], v[72:75], v[68:71]
	v_add_u32_e32 v72, 24, v67
	v_bitop3_b32 v72, v72, v155, 15 bitop3:0x78
	v_lshl_add_u32 v76, v72, 4, v80
	v_add_u32_e32 v72, 0, v76
	ds_read_b128 v[72:75], v72
	v_add_u32_e32 v76, s21, v76
	ds_read_b128 v[76:79], v76
	s_waitcnt lgkmcnt(1)
	v_mfma_f32_16x16x32_bf16 v[68:71], v[50:53], v[72:75], v[68:71]
	v_add_u32_e32 v67, 28, v67
	v_bitop3_b32 v67, v67, v155, 15 bitop3:0x78
	v_lshl_add_u32 v67, v67, 4, v80
	s_waitcnt lgkmcnt(0)
	v_mfma_f32_16x16x32_bf16 v[68:71], v[50:53], v[76:79], v[68:71]
	v_mfma_f32_16x16x32_bf16 v[68:71], v[54:57], v[72:75], v[68:71]
	v_add_u32_e32 v72, 0, v67
	ds_read_b128 v[72:75], v72
	v_add_u32_e32 v67, s21, v67
	ds_read_b128 v[76:79], v67
	s_waitcnt lgkmcnt(1)
	v_mfma_f32_16x16x32_bf16 v[68:71], v[58:61], v[72:75], v[68:71]
	v_lshlrev_b32_e32 v67, 6, v66
	s_waitcnt lgkmcnt(0)
	s_barrier
	v_mfma_f32_16x16x32_bf16 v[68:71], v[58:61], v[76:79], v[68:71]
	v_mfma_f32_16x16x32_bf16 v[68:71], v[62:65], v[72:75], v[68:71]
	v_and_b32_e32 v72, -16, v155
	v_add3_u32 v67, s18, v67, v72
	v_bfe_u32 v72, v155, 4, 1
	v_cmp_eq_u32_e64 s[6:7], 0, v72
	s_and_b64 s[22:23], vcc, s[6:7]
	s_nop 2
	ds_write_b128 v67, v[68:71]
	v_lshlrev_b32_e32 v69, 7, v155
	v_lshl_add_u32 v67, v72, 6, s19
	v_lshlrev_b32_e32 v68, 2, v66
	v_and_b32_e32 v69, 0xfffff000, v69
	v_add3_u32 v67, v67, v68, v69
	s_waitcnt lgkmcnt(0)
	s_barrier
	ds_read2st64_b32 v[68:69], v67 offset1:4
	ds_read2st64_b32 v[70:71], v67 offset0:8 offset1:12
	s_waitcnt lgkmcnt(1)
	v_add_f32_e32 v67, 0, v68
	v_add_f32_e32 v67, v67, v69
	s_waitcnt lgkmcnt(0)
	v_add_f32_e32 v67, v67, v70
	v_add_f32_e32 v67, v67, v71
	ds_bpermute_b32 v68, v153, v67
	s_waitcnt lgkmcnt(0)
	v_add_f32_e32 v67, v67, v68
	ds_bpermute_b32 v68, v148, v67
	s_waitcnt lgkmcnt(0)
	v_max_f32_e32 v68, v68, v68
	v_max_f32_e32 v68, v67, v68
	ds_bpermute_b32 v69, v149, v68
	s_waitcnt lgkmcnt(0)
	v_max_f32_e32 v69, v69, v69
	v_max_f32_e32 v68, v68, v69
	ds_bpermute_b32 v69, v150, v68
	s_waitcnt lgkmcnt(0)
	v_max_f32_e32 v69, v69, v69
	v_max_f32_e32 v68, v68, v69
	ds_bpermute_b32 v69, v151, v68
	s_waitcnt lgkmcnt(0)
	v_max_f32_e32 v69, v69, v69
	v_max_f32_e32 v68, v68, v69
	v_sub_f32_e32 v67, v67, v68
	v_mul_f32_e32 v67, 0x3fb8aa3b, v67
	v_exp_f32_e32 v67, v67
	ds_bpermute_b32 v68, v148, v67
	s_waitcnt lgkmcnt(0)
	v_add_f32_e32 v68, v67, v68
	ds_bpermute_b32 v69, v149, v68
	s_waitcnt lgkmcnt(0)
	v_add_f32_e32 v68, v68, v69
	ds_bpermute_b32 v69, v150, v68
	s_waitcnt lgkmcnt(0)
	v_add_f32_e32 v68, v68, v69
	ds_bpermute_b32 v69, v151, v68
	s_and_saveexec_b64 s[6:7], s[22:23]
	s_cbranch_execz .LBB0_1820
	s_waitcnt lgkmcnt(0)
	v_add_f32_e32 v68, v68, v69
	v_div_scale_f32 v69, s[22:23], v68, v68, v67
	v_rcp_f32_e32 v70, v69
	v_div_scale_f32 v71, vcc, v67, v68, v67
	v_mul_u32_u24_e32 v66, 0x4100, v66
	v_fma_f32 v72, -v69, v70, 1.0
	v_fmac_f32_e32 v70, v72, v70
	v_mul_f32_e32 v72, v71, v70
	v_fma_f32 v73, -v69, v72, v71
	v_fmac_f32_e32 v72, v73, v70
	v_fma_f32 v69, -v69, v72, v71
	v_div_fmas_f32 v69, v69, v70, v72
	s_add_u32 s22, s8, s0
	v_div_fixup_f32 v67, v69, v68, v67
	v_lshlrev_b32_e32 v66, 2, v66
	s_addc_u32 s23, s9, s20
	global_store_dword v66, v67, s[22:23]
	s_branch .LBB0_1820

.LBB0_2297:
	v_lshlrev_b64 v[66:67], 13, v[66:67]
	s_waitcnt vmcnt(7)
	v_lshlrev_b32_e32 v116, 16, v98
	v_and_b32_e32 v117, 0xffff0000, v98
	v_lshlrev_b32_e32 v98, 16, v99
	v_and_b32_e32 v99, 0xffff0000, v99
	s_waitcnt vmcnt(5)
	v_lshlrev_b32_e32 v120, 16, v92
	v_and_b32_e32 v121, 0xffff0000, v92
	s_waitcnt vmcnt(2)
	v_lshlrev_b32_e32 v130, 16, v84
	v_and_b32_e32 v131, 0xffff0000, v84
	v_lshl_add_u64 v[66:67], s[4:5], 0, v[66:67]
	v_lshlrev_b32_e32 v118, 16, v96
	v_and_b32_e32 v119, 0xffff0000, v96
	v_lshlrev_b32_e32 v96, 16, v97
	v_and_b32_e32 v97, 0xffff0000, v97
	v_lshlrev_b32_e32 v92, 16, v93
	v_and_b32_e32 v93, 0xffff0000, v93
	v_lshlrev_b32_e32 v122, 16, v90
	v_and_b32_e32 v123, 0xffff0000, v90
	v_lshlrev_b32_e32 v124, 16, v91
	v_and_b32_e32 v125, 0xffff0000, v91
	v_lshlrev_b32_e32 v126, 16, v86
	v_and_b32_e32 v127, 0xffff0000, v86
	v_lshlrev_b32_e32 v128, 16, v87
	v_and_b32_e32 v129, 0xffff0000, v87
	s_waitcnt vmcnt(1)
	v_lshlrev_b32_e32 v136, 16, v80
	v_and_b32_e32 v137, 0xffff0000, v80
	v_lshlrev_b32_e32 v138, 16, v81
	v_and_b32_e32 v139, 0xffff0000, v81
	s_waitcnt vmcnt(0)
	v_lshlrev_b32_e32 v140, 16, v78
	v_and_b32_e32 v141, 0xffff0000, v78
	v_lshlrev_b32_e32 v142, 16, v79
	v_and_b32_e32 v143, 0xffff0000, v79
	s_waitcnt lgkmcnt(7)
	v_pk_fma_f32 v[80:81], v[114:115], v[2:3], v[98:99]
	v_pk_fma_f32 v[78:79], v[110:111], v[0:1], v[116:117]
	s_waitcnt lgkmcnt(5)
	v_pk_fma_f32 v[90:91], v[104:105], v[8:9], v[120:121]
	s_waitcnt lgkmcnt(2)
	v_pk_fma_f32 v[104:105], v[76:77], v[20:21], v[130:131]
	v_lshl_add_u64 v[76:77], v[66:67], 0, v[34:35]
	v_mov_b32_e32 v43, v35
	v_lshlrev_b32_e32 v132, 16, v85
	v_and_b32_e32 v133, 0xffff0000, v85
	v_pk_fma_f32 v[86:87], v[112:113], v[6:7], v[96:97]
	v_pk_fma_f32 v[84:85], v[108:109], v[4:5], v[118:119]
	v_pk_fma_f32 v[92:93], v[106:107], v[10:11], v[92:93]
	v_pk_fma_f32 v[98:99], v[102:103], v[14:15], v[124:125]
	v_pk_fma_f32 v[96:97], v[100:101], v[12:13], v[122:123]
	v_pk_fma_f32 v[102:103], v[94:95], v[18:19], v[128:129]
	v_pk_fma_f32 v[100:101], v[88:89], v[16:17], v[126:127]
	global_store_dwordx4 v[76:77], v[78:81], off nt
	global_store_dwordx4 v[76:77], v[84:87], off offset:1024 nt
	global_store_dwordx4 v[76:77], v[90:93], off offset:2048 nt
	global_store_dwordx4 v[76:77], v[96:99], off offset:3072 nt
	v_lshl_add_u64 v[76:77], v[66:67], 0, v[42:43]
	v_mov_b32_e32 v45, v35
	s_and_b64 s[0:1], exec, s[0:1]
	v_pk_fma_f32 v[106:107], v[82:83], v[22:23], v[132:133]
	global_store_dwordx4 v[76:77], v[100:103], off nt
	v_lshl_add_u64 v[76:77], v[66:67], 0, v[44:45]
	v_mov_b32_e32 v47, v35
	v_mov_b32_e32 v49, v35
	s_or_b64 s[6:7], s[0:1], s[6:7]
	s_waitcnt lgkmcnt(1)
	v_pk_fma_f32 v[74:75], v[74:75], v[26:27], v[138:139]
	v_pk_fma_f32 v[72:73], v[72:73], v[24:25], v[136:137]
	s_waitcnt lgkmcnt(0)
	v_pk_fma_f32 v[70:71], v[70:71], v[30:31], v[142:143]
	v_pk_fma_f32 v[68:69], v[68:69], v[28:29], v[140:141]
	global_store_dwordx4 v[76:77], v[104:107], off nt
	v_lshl_add_u64 v[76:77], v[66:67], 0, v[46:47]
	v_lshl_add_u64 v[66:67], v[66:67], 0, v[48:49]
	v_mov_b32_e32 v43, v33
	global_store_dwordx4 v[76:77], v[72:75], off nt
	global_store_dwordx4 v[66:67], v[68:71], off nt
	s_andn2_b64 exec, exec, s[6:7]
	s_cbranch_execz .LBB0_2307
